# k6_attn_trim2
# speedup vs baseline: 1.0031x; 1.0031x over previous
.LBB1_14:
	v_add_u32_e32 v203, s30, v240
	ds_read_b64_tr_b16 v[196:197], v203 offset:24576
	ds_read_b64_tr_b16 v[198:199], v203 offset:25088
	s_waitcnt lgkmcnt(9)
	v_mfma_f32_32x32x16_f16 v[112:127], v[192:195], v[148:151], v[48:63]
	v_cvt_pk_f16_f32 v156, v80, v81
	v_cvt_pk_f16_f32 v157, v82, v83
	ds_read_b64_tr_b16 v[192:193], v203 offset:28672
	ds_read_b64_tr_b16 v[194:195], v203 offset:29184
	s_waitcnt lgkmcnt(10)
	v_mfma_f32_32x32x16_f16 v[96:111], v[188:191], v[148:151], v[48:63]
	v_cvt_pk_f16_f32 v158, v84, v85
	v_cvt_pk_f16_f32 v159, v86, v87
	ds_read_b64_tr_b16 v[188:189], v203 offset:25600
	ds_read_b64_tr_b16 v[190:191], v203 offset:26112
	s_waitcnt lgkmcnt(11)
	v_mfma_f32_32x32x16_f16 v[112:127], v[184:187], v[140:143], v[112:127]
	v_cvt_pk_f16_f32 v160, v88, v89
	v_cvt_pk_f16_f32 v161, v90, v91
	ds_read_b64_tr_b16 v[88:89], v203 offset:29696
	ds_read_b64_tr_b16 v[90:91], v203 offset:30208
	s_waitcnt lgkmcnt(12)
	v_mfma_f32_32x32x16_f16 v[96:111], v[176:179], v[140:143], v[96:111]
	v_cvt_pk_f16_f32 v162, v92, v93
	v_cvt_pk_f16_f32 v163, v94, v95
	ds_read_b64_tr_b16 v[84:85], v203 offset:26624
	ds_read_b64_tr_b16 v[86:87], v203 offset:27136
	s_waitcnt lgkmcnt(13)
	v_mfma_f32_32x32x16_f16 v[112:127], v[180:183], v[136:139], v[112:127]
	v_cvt_pk_f16_f32 v152, v64, v65
	v_cvt_pk_f16_f32 v153, v66, v67
	v_pk_add_f16 v252, v156, v160
	v_add_u32_e32 v92, s45, v243
	ds_read_b64_tr_b16 v[80:81], v203 offset:30720
	ds_read_b64_tr_b16 v[82:83], v203 offset:31232
	s_waitcnt lgkmcnt(14)
	v_mfma_f32_32x32x16_f16 v[96:111], v[172:175], v[136:139], v[96:111]
	v_cvt_pk_f16_f32 v154, v68, v69
	v_cvt_pk_f16_f32 v155, v70, v71
	v_pk_add_f16 v253, v157, v161
	ds_read_b64_tr_b16 v[68:69], v203 offset:27648
	ds_read_b64_tr_b16 v[70:71], v203 offset:28160
	s_waitcnt lgkmcnt(14)
	v_mfma_f32_32x32x16_f16 v[112:127], v[168:171], v[132:135], v[112:127]
	v_cvt_pk_f16_f32 v144, v72, v73
	v_cvt_pk_f16_f32 v145, v74, v75
	v_pk_add_f16 v254, v158, v162
	ds_read_b64_tr_b16 v[64:65], v203 offset:31744
	ds_read_b64_tr_b16 v[66:67], v203 offset:32256
	v_mfma_f32_32x32x16_f16 v[96:111], v[164:167], v[132:135], v[96:111]
	v_cvt_pk_f16_f32 v146, v76, v77
	v_cvt_pk_f16_f32 v147, v78, v79
	v_pk_add_f16 v255, v159, v163
	s_add_i32 m0, s48, s38
	s_add_u32 s56, s52, 0x80000
	s_addc_u32 s57, s53, 0
	global_load_lds_dwordx4 v200, s[56:57]
	s_add_i32 m0, m0, 0xfc0
	s_add_u32 s58, s54, 0x40000
	s_addc_u32 s59, s55, 0
	global_load_lds_dwordx4 v200, s[56:57] offset:64
	s_add_i32 m0, s45, s39
	s_nop 0
	global_load_lds_dwordx4 v250, s[58:59]
	s_add_i32 m0, m0, 0xfc0
	s_nop 0
	global_load_lds_dwordx4 v250, s[58:59] offset:64
	v_max_f32_e32 v72, v112, v113
	v_max3_f32 v73, v114, v115, v97
	v_max3_f32 v72, v72, v96, v98
	v_max3_f32 v72, v72, v99, v116
	v_max3_f32 v73, v73, v118, v119
	v_max3_f32 v72, v72, v117, v100
	v_max3_f32 v73, v73, v102, v103
	v_max3_f32 v72, v72, v101, v120
	v_max3_f32 v73, v73, v122, v123
	v_max3_f32 v72, v72, v121, v104
	v_max3_f32 v73, v73, v106, v107
	v_max3_f32 v72, v72, v105, v124
	v_max3_f32 v73, v73, v126, v127
	v_max3_f32 v72, v72, v125, v108
	v_max3_f32 v73, v73, v110, v111
	v_max3_f32 v72, v72, v109, v73
	v_mov_b32_e32 v73, v72
	s_nop 1
	v_permlane32_swap_b32_e32 v72, v73
	v_max_f32_e32 v72, v72, v73
	v_cmp_lt_f32_e32 vcc, s47, v72
	s_cmp_lg_u64 vcc, 0
	s_cselect_b64 s[30:31], -1, 0
	s_cbranch_vccnz .LBB1_22
.LBB1_15:
	s_waitcnt lgkmcnt(14)
	v_mfma_f32_32x32x16_f16 v[0:15], v[156:159], v[196:199], v[0:15]
	v_exp_f32_e32 v112, v112
	v_exp_f32_e32 v113, v113
	v_exp_f32_e32 v114, v114
	v_exp_f32_e32 v115, v115
	s_waitcnt lgkmcnt(12)
	v_mfma_f32_32x32x16_f16 v[16:31], v[156:159], v[192:195], v[16:31]
	v_exp_f32_e32 v116, v116
	v_exp_f32_e32 v117, v117
	v_exp_f32_e32 v118, v118
	v_exp_f32_e32 v119, v119
	ds_read_b128 v[72:75], v92
	ds_read_b128 v[180:183], v92 offset:512
	s_waitcnt lgkmcnt(12)
	v_mfma_f32_32x32x16_f16 v[0:15], v[160:163], v[188:191], v[0:15]
	v_exp_f32_e32 v120, v120
	v_exp_f32_e32 v121, v121
	v_exp_f32_e32 v122, v122
	v_exp_f32_e32 v123, v123
	ds_read_b128 v[184:187], v92 offset:2048
	ds_read_b128 v[168:171], v92 offset:2560
	s_waitcnt lgkmcnt(12)
	v_mfma_f32_32x32x16_f16 v[16:31], v[160:163], v[88:91], v[16:31]
	v_exp_f32_e32 v124, v124
	v_exp_f32_e32 v125, v125
	v_exp_f32_e32 v126, v126
	v_exp_f32_e32 v127, v127
	v_pk_add_f16 v88, v152, v144
	v_pk_add_f16 v89, v153, v145
	v_pk_add_f16 v90, v154, v146
	v_pk_add_f16 v91, v155, v147
	v_pk_add_f16 v78, v254, v90
	v_pk_add_f16 v79, v255, v91
	v_pk_add_f16 v77, v253, v89
	v_pk_add_f16 v76, v252, v88
	s_nop 1
	v_mfma_f32_32x32x16_f16 v[32:47], v[76:79], v[128:131], v[32:47]
	ds_read_b128 v[188:191], v92 offset:4096
	ds_read_b128 v[172:175], v92 offset:4608
	s_waitcnt lgkmcnt(12)
	v_mfma_f32_32x32x16_f16 v[0:15], v[152:155], v[84:87], v[0:15]
	v_exp_f32_e32 v96, v96
	v_exp_f32_e32 v97, v97
	v_exp_f32_e32 v98, v98
	v_exp_f32_e32 v99, v99
	ds_read_b128 v[176:179], v92 offset:6144
	ds_read_b128 v[164:167], v92 offset:6656
	s_waitcnt lgkmcnt(12)
	v_mfma_f32_32x32x16_f16 v[16:31], v[152:155], v[80:83], v[16:31]
	v_exp_f32_e32 v100, v100
	v_exp_f32_e32 v101, v101
	v_exp_f32_e32 v102, v102
	v_exp_f32_e32 v103, v103
	s_waitcnt lgkmcnt(10)
	v_mfma_f32_32x32x16_f16 v[0:15], v[144:147], v[68:71], v[0:15]
	v_exp_f32_e32 v104, v104
	v_exp_f32_e32 v105, v105
	v_exp_f32_e32 v106, v106
	v_exp_f32_e32 v107, v107
	s_waitcnt lgkmcnt(8)
	v_mfma_f32_32x32x16_f16 v[16:31], v[144:147], v[64:67], v[16:31]
	v_exp_f32_e32 v108, v108
	v_exp_f32_e32 v109, v109
	v_exp_f32_e32 v110, v110
	v_exp_f32_e32 v111, v111
	s_waitcnt vmcnt(4) lgkmcnt(0)
	s_barrier
	s_andn2_b64 vcc, exec, s[30:31]
	s_cbranch_vccnz .LBB1_17
	ds_read_b128 v[64:67], v201 offset:49248
	ds_read_b128 v[68:71], v201 offset:49216
	ds_read_b128 v[76:79], v201 offset:49184
	ds_read_b128 v[80:83], v201 offset:49152
	s_waitcnt lgkmcnt(3)
	v_pk_mul_f32 v[12:13], v[12:13], v[64:65]
	s_waitcnt lgkmcnt(2)
	v_pk_mul_f32 v[8:9], v[8:9], v[68:69]
	s_waitcnt lgkmcnt(1)
	v_pk_mul_f32 v[4:5], v[4:5], v[76:77]
	v_pk_mul_f32 v[14:15], v[14:15], v[66:67]
	v_pk_mul_f32 v[10:11], v[10:11], v[70:71]
	v_pk_mul_f32 v[6:7], v[6:7], v[78:79]
	s_waitcnt lgkmcnt(0)
	v_pk_mul_f32 v[2:3], v[2:3], v[82:83]
	v_pk_mul_f32 v[0:1], v[0:1], v[80:81]
	v_pk_mul_f32 v[28:29], v[28:29], v[64:65]
	v_pk_mul_f32 v[24:25], v[24:25], v[68:69]
	v_pk_mul_f32 v[20:21], v[20:21], v[76:77]
	v_pk_mul_f32 v[30:31], v[30:31], v[66:67]
	v_pk_mul_f32 v[26:27], v[26:27], v[70:71]
	v_pk_mul_f32 v[22:23], v[22:23], v[78:79]
	v_pk_mul_f32 v[18:19], v[18:19], v[82:83]
	v_pk_mul_f32 v[16:17], v[16:17], v[80:81]
	v_pk_mul_f32 v[44:45], v[44:45], v[64:65]
	v_pk_mul_f32 v[40:41], v[40:41], v[68:69]
	v_pk_mul_f32 v[36:37], v[36:37], v[76:77]
	v_pk_mul_f32 v[46:47], v[46:47], v[66:67]
	v_pk_mul_f32 v[42:43], v[42:43], v[70:71]
	v_pk_mul_f32 v[38:39], v[38:39], v[78:79]
	v_pk_mul_f32 v[34:35], v[34:35], v[82:83]
	v_pk_mul_f32 v[32:33], v[32:33], v[80:81]
.LBB1_17:
	s_add_i32 s30, s45, 0x2000
	s_cmpk_lg_i32 s45, 0x4000
	s_cselect_b32 s41, s30, 0
	v_add_u32_e32 v203, s48, v240
	ds_read_b64_tr_b16 v[196:197], v203 offset:24576
	ds_read_b64_tr_b16 v[198:199], v203 offset:25088
	s_waitcnt lgkmcnt(9)
	v_mfma_f32_32x32x16_f16 v[80:95], v[72:75], v[148:151], v[48:63]
	v_cvt_pk_f16_f32 v156, v112, v113
	v_cvt_pk_f16_f32 v157, v114, v115
	ds_read_b64_tr_b16 v[192:193], v203 offset:28672
	ds_read_b64_tr_b16 v[194:195], v203 offset:29184
	s_waitcnt lgkmcnt(10)
	v_mfma_f32_32x32x16_f16 v[64:79], v[180:183], v[148:151], v[48:63]
	v_cvt_pk_f16_f32 v158, v116, v117
	v_cvt_pk_f16_f32 v159, v118, v119
	ds_read_b64_tr_b16 v[180:181], v203 offset:25600
	ds_read_b64_tr_b16 v[182:183], v203 offset:26112
	s_waitcnt lgkmcnt(11)
	v_mfma_f32_32x32x16_f16 v[80:95], v[184:187], v[140:143], v[80:95]
	v_cvt_pk_f16_f32 v160, v120, v121
	v_cvt_pk_f16_f32 v161, v122, v123
	ds_read_b64_tr_b16 v[120:121], v203 offset:29696
	ds_read_b64_tr_b16 v[122:123], v203 offset:30208
	s_waitcnt lgkmcnt(12)
	v_mfma_f32_32x32x16_f16 v[64:79], v[168:171], v[140:143], v[64:79]
	v_cvt_pk_f16_f32 v162, v124, v125
	v_cvt_pk_f16_f32 v163, v126, v127
	ds_read_b64_tr_b16 v[116:117], v203 offset:26624
	ds_read_b64_tr_b16 v[118:119], v203 offset:27136
	s_waitcnt lgkmcnt(13)
	v_mfma_f32_32x32x16_f16 v[80:95], v[188:191], v[136:139], v[80:95]
	v_cvt_pk_f16_f32 v152, v96, v97
	v_cvt_pk_f16_f32 v153, v98, v99
	v_pk_add_f16 v252, v156, v160
	ds_read_b64_tr_b16 v[112:113], v203 offset:30720
	ds_read_b64_tr_b16 v[114:115], v203 offset:31232
	s_waitcnt lgkmcnt(14)
	v_mfma_f32_32x32x16_f16 v[64:79], v[172:175], v[136:139], v[64:79]
	v_cvt_pk_f16_f32 v154, v100, v101
	v_cvt_pk_f16_f32 v155, v102, v103
	v_pk_add_f16 v253, v157, v161
	ds_read_b64_tr_b16 v[100:101], v203 offset:27648
	ds_read_b64_tr_b16 v[102:103], v203 offset:28160
	s_waitcnt lgkmcnt(14)
	v_mfma_f32_32x32x16_f16 v[80:95], v[176:179], v[132:135], v[80:95]
	v_cvt_pk_f16_f32 v144, v104, v105
	v_cvt_pk_f16_f32 v145, v106, v107
	v_pk_add_f16 v254, v158, v162
	ds_read_b64_tr_b16 v[96:97], v203 offset:31744
	ds_read_b64_tr_b16 v[98:99], v203 offset:32256
	v_mfma_f32_32x32x16_f16 v[64:79], v[164:167], v[132:135], v[64:79]
	v_cvt_pk_f16_f32 v146, v108, v109
	v_cvt_pk_f16_f32 v147, v110, v111
	v_pk_add_f16 v255, v159, v163
	s_add_i32 m0, s45, s38
	s_add_u32 s56, s52, 0xa0000
	s_addc_u32 s57, s53, 0
	global_load_lds_dwordx4 v200, s[56:57]
	s_add_i32 m0, m0, 0xfc0
	s_add_u32 s58, s54, 0x60000
	s_addc_u32 s59, s55, 0
	global_load_lds_dwordx4 v200, s[56:57] offset:64
	s_add_i32 m0, s41, s39
	s_nop 0
	global_load_lds_dwordx4 v250, s[58:59]
	s_add_i32 m0, m0, 0xfc0
	s_nop 0
	global_load_lds_dwordx4 v250, s[58:59] offset:64
	v_max_f32_e32 v104, v80, v81
	v_max3_f32 v105, v82, v83, v65
	v_max3_f32 v104, v104, v64, v66
	v_max3_f32 v104, v104, v67, v84
	v_max3_f32 v105, v105, v86, v87
	v_max3_f32 v104, v104, v85, v68
	v_max3_f32 v105, v105, v70, v71
	v_max3_f32 v104, v104, v69, v88
	v_max3_f32 v105, v105, v90, v91
	v_max3_f32 v104, v104, v89, v72
	v_max3_f32 v105, v105, v74, v75
	v_max3_f32 v104, v104, v73, v92
	v_max3_f32 v105, v105, v94, v95
	v_max3_f32 v104, v104, v93, v76
	v_max3_f32 v105, v105, v78, v79
	v_max3_f32 v104, v104, v77, v105
	v_mov_b32_e32 v105, v104
	s_nop 1
	v_permlane32_swap_b32_e32 v104, v105
	v_max_f32_e32 v104, v104, v105
	v_cmp_lt_f32_e32 vcc, s47, v104
	s_cmp_lg_u64 vcc, 0
	s_cselect_b64 s[30:31], -1, 0
	s_cbranch_vccnz .LBB1_25
.LBB1_18:
	s_waitcnt lgkmcnt(14)
	v_mfma_f32_32x32x16_f16 v[0:15], v[156:159], v[196:199], v[0:15]
	v_exp_f32_e32 v80, v80
	v_exp_f32_e32 v81, v81
	v_exp_f32_e32 v82, v82
	v_exp_f32_e32 v83, v83
	s_waitcnt lgkmcnt(12)
	v_mfma_f32_32x32x16_f16 v[16:31], v[156:159], v[192:195], v[16:31]
	v_exp_f32_e32 v84, v84
	v_exp_f32_e32 v85, v85
	v_exp_f32_e32 v86, v86
	v_exp_f32_e32 v87, v87
	v_add_u32_e32 v108, s41, v243
	ds_read_b128 v[192:195], v108
	ds_read_b128 v[188:191], v108 offset:512
	s_waitcnt lgkmcnt(12)
	v_mfma_f32_32x32x16_f16 v[0:15], v[160:163], v[180:183], v[0:15]
	v_exp_f32_e32 v88, v88
	v_exp_f32_e32 v89, v89
	v_exp_f32_e32 v90, v90
	v_exp_f32_e32 v91, v91
	ds_read_b128 v[184:187], v108 offset:2048
	ds_read_b128 v[176:179], v108 offset:2560
	s_waitcnt lgkmcnt(12)
	v_mfma_f32_32x32x16_f16 v[16:31], v[160:163], v[120:123], v[16:31]
	v_exp_f32_e32 v92, v92
	v_exp_f32_e32 v93, v93
	v_exp_f32_e32 v94, v94
	v_exp_f32_e32 v95, v95
	v_pk_add_f16 v109, v152, v144
	v_pk_add_f16 v110, v153, v145
	v_pk_add_f16 v111, v154, v146
	v_pk_add_f16 v120, v155, v147
	v_pk_add_f16 v106, v254, v111
	v_pk_add_f16 v107, v255, v120
	v_pk_add_f16 v105, v253, v110
	v_pk_add_f16 v104, v252, v109
	s_nop 1
	v_mfma_f32_32x32x16_f16 v[32:47], v[104:107], v[128:131], v[32:47]
	ds_read_b128 v[180:183], v108 offset:4096
	ds_read_b128 v[172:175], v108 offset:4608
	s_waitcnt lgkmcnt(12)
	v_mfma_f32_32x32x16_f16 v[0:15], v[152:155], v[116:119], v[0:15]
	v_exp_f32_e32 v64, v64
	v_exp_f32_e32 v65, v65
	v_exp_f32_e32 v66, v66
	v_exp_f32_e32 v67, v67
	ds_read_b128 v[168:171], v108 offset:6144
	ds_read_b128 v[164:167], v108 offset:6656
	s_waitcnt lgkmcnt(12)
	v_mfma_f32_32x32x16_f16 v[16:31], v[152:155], v[112:115], v[16:31]
	v_exp_f32_e32 v68, v68
	v_exp_f32_e32 v69, v69
	v_exp_f32_e32 v70, v70
	v_exp_f32_e32 v71, v71
	s_waitcnt lgkmcnt(10)
	v_mfma_f32_32x32x16_f16 v[0:15], v[144:147], v[100:103], v[0:15]
	v_exp_f32_e32 v72, v72
	v_exp_f32_e32 v73, v73
	v_exp_f32_e32 v74, v74
	v_exp_f32_e32 v75, v75
	s_waitcnt lgkmcnt(8)
	v_mfma_f32_32x32x16_f16 v[16:31], v[144:147], v[96:99], v[16:31]
	v_exp_f32_e32 v76, v76
	v_exp_f32_e32 v77, v77
	v_exp_f32_e32 v78, v78
	v_exp_f32_e32 v79, v79
	s_waitcnt vmcnt(4) lgkmcnt(0)
	s_barrier
	s_andn2_b64 vcc, exec, s[30:31]
	s_cbranch_vccnz .LBB1_20
	ds_read_b128 v[96:99], v201 offset:49248
	ds_read_b128 v[100:103], v201 offset:49216
	ds_read_b128 v[104:107], v201 offset:49184
	ds_read_b128 v[108:111], v201 offset:49152
	s_waitcnt lgkmcnt(3)
	v_pk_mul_f32 v[12:13], v[12:13], v[96:97]
	s_waitcnt lgkmcnt(2)
	v_pk_mul_f32 v[8:9], v[8:9], v[100:101]
	s_waitcnt lgkmcnt(1)
	v_pk_mul_f32 v[4:5], v[4:5], v[104:105]
	v_pk_mul_f32 v[14:15], v[14:15], v[98:99]
	v_pk_mul_f32 v[10:11], v[10:11], v[102:103]
	v_pk_mul_f32 v[6:7], v[6:7], v[106:107]
	s_waitcnt lgkmcnt(0)
	v_pk_mul_f32 v[2:3], v[2:3], v[110:111]
	v_pk_mul_f32 v[0:1], v[0:1], v[108:109]
	v_pk_mul_f32 v[28:29], v[28:29], v[96:97]
	v_pk_mul_f32 v[24:25], v[24:25], v[100:101]
	v_pk_mul_f32 v[20:21], v[20:21], v[104:105]
	v_pk_mul_f32 v[30:31], v[30:31], v[98:99]
	v_pk_mul_f32 v[26:27], v[26:27], v[102:103]
	v_pk_mul_f32 v[22:23], v[22:23], v[106:107]
	v_pk_mul_f32 v[18:19], v[18:19], v[110:111]
	v_pk_mul_f32 v[16:17], v[16:17], v[108:109]
	v_pk_mul_f32 v[44:45], v[44:45], v[96:97]
	v_pk_mul_f32 v[40:41], v[40:41], v[100:101]
	v_pk_mul_f32 v[36:37], v[36:37], v[104:105]
	v_pk_mul_f32 v[46:47], v[46:47], v[98:99]
	v_pk_mul_f32 v[42:43], v[42:43], v[102:103]
	v_pk_mul_f32 v[38:39], v[38:39], v[106:107]
	v_pk_mul_f32 v[34:35], v[34:35], v[110:111]
	v_pk_mul_f32 v[32:33], v[32:33], v[108:109]

	.amdhsa_kernel _Z10attn64_fwdPKDF16_S0_S0_PDF16_
		.amdhsa_group_segment_fixed_size 0
		.amdhsa_private_segment_fixed_size 0
		.amdhsa_kernarg_size 32
		.amdhsa_user_sgpr_count 2
		.amdhsa_user_sgpr_dispatch_ptr 0
		.amdhsa_user_sgpr_queue_ptr 0
		.amdhsa_user_sgpr_kernarg_segment_ptr 1
		.amdhsa_user_sgpr_dispatch_id 0
		.amdhsa_user_sgpr_kernarg_preload_length 0
		.amdhsa_user_sgpr_kernarg_preload_offset 0
		.amdhsa_user_sgpr_private_segment_size 0
		.amdhsa_uses_dynamic_stack 0
		.amdhsa_enable_private_segment 0
		.amdhsa_system_sgpr_workgroup_id_x 1
		.amdhsa_system_sgpr_workgroup_id_y 0
		.amdhsa_system_sgpr_workgroup_id_z 0
		.amdhsa_system_sgpr_workgroup_info 0
		.amdhsa_system_vgpr_workitem_id 0
		.amdhsa_next_free_vgpr 256
		.amdhsa_next_free_sgpr 60
		.amdhsa_accum_offset 256
		.amdhsa_reserve_vcc 1
		.amdhsa_float_round_mode_32 0
		.amdhsa_float_round_mode_16_64 0
		.amdhsa_float_denorm_mode_32 3
		.amdhsa_float_denorm_mode_16_64 3
		.amdhsa_dx10_clamp 1
		.amdhsa_ieee_mode 1
		.amdhsa_fp16_overflow 0
		.amdhsa_tg_split 0
		.amdhsa_exception_fp_ieee_invalid_op 0
		.amdhsa_exception_fp_denorm_src 0
		.amdhsa_exception_fp_ieee_div_zero 0
		.amdhsa_exception_fp_ieee_overflow 0
		.amdhsa_exception_fp_ieee_underflow 0
		.amdhsa_exception_fp_ieee_inexact 0
		.amdhsa_exception_int_div_zero 0
	.end_amdhsa_kernel

amdhsa.kernels:
  - .agpr_count:     0
    .args:
      - .address_space:  global
        .offset:         0
        .size:           8
        .value_kind:     global_buffer
      - .address_space:  global
        .offset:         8
        .size:           8
        .value_kind:     global_buffer
      - .address_space:  global
        .offset:         16
        .size:           8
        .value_kind:     global_buffer
      - .address_space:  global
        .offset:         24
        .size:           8
        .value_kind:     global_buffer
      - .address_space:  global
        .offset:         32
        .size:           8
        .value_kind:     global_buffer
      - .actual_access:  write_only
        .address_space:  global
        .offset:         40
        .size:           8
        .value_kind:     global_buffer
      - .actual_access:  write_only
        .address_space:  global
        .offset:         48
        .size:           8
        .value_kind:     global_buffer
      - .actual_access:  write_only
        .address_space:  global
        .offset:         56
        .size:           8
        .value_kind:     global_buffer
      - .actual_access:  write_only
        .address_space:  global
        .offset:         64
        .size:           8
        .value_kind:     global_buffer
    .group_segment_fixed_size: 0
    .kernarg_segment_align: 8
    .kernarg_segment_size: 72
    .language:       OpenCL C
    .language_version:
      - 2
      - 0
    .max_flat_workgroup_size: 256
    .name:           _Z11prep_kernelPKfS0_S0_S0_S0_PDF16_S1_S1_P15HIP_vector_typeIfLj2EE
    .private_segment_fixed_size: 0
    .sgpr_count:     38
    .sgpr_spill_count: 0
    .symbol:         _Z11prep_kernelPKfS0_S0_S0_S0_PDF16_S1_S1_P15HIP_vector_typeIfLj2EE.kd
    .uniform_work_group_size: 1
    .uses_dynamic_stack: false
    .vgpr_count:     44
    .vgpr_spill_count: 0
    .wavefront_size: 64
  - .agpr_count:     0
    .args:
      - .address_space:  global
        .offset:         0
        .size:           8
        .value_kind:     global_buffer
      - .address_space:  global
        .offset:         8
        .size:           8
        .value_kind:     global_buffer
      - .address_space:  global
        .offset:         16
        .size:           8
        .value_kind:     global_buffer
      - .address_space:  global
        .offset:         24
        .size:           8
        .value_kind:     global_buffer
    .group_segment_fixed_size: 0
    .kernarg_segment_align: 8
    .kernarg_segment_size: 32
    .language:       OpenCL C
    .language_version:
      - 2
      - 0
    .max_flat_workgroup_size: 256
    .name:           _Z10attn64_fwdPKDF16_S0_S0_PDF16_
    .private_segment_fixed_size: 0
    .sgpr_count:     66
    .sgpr_spill_count: 0
    .symbol:         _Z10attn64_fwdPKDF16_S0_S0_PDF16_.kd
    .uniform_work_group_size: 1
    .uses_dynamic_stack: false
    .vgpr_count:     256
    .vgpr_spill_count: 0
    .wavefront_size: 64
  - .agpr_count:     0
    .args:
      - .address_space:  global
        .offset:         0
        .size:           8
        .value_kind:     global_buffer
      - .address_space:  global
        .offset:         8
        .size:           8
        .value_kind:     global_buffer
      - .actual_access:  read_only
        .address_space:  global
        .offset:         16
        .size:           8
        .value_kind:     global_buffer
      - .actual_access:  write_only
        .address_space:  global
        .offset:         24
        .size:           8
        .value_kind:     global_buffer
      - .actual_access:  write_only
        .address_space:  global
        .offset:         32
        .size:           8
        .value_kind:     global_buffer
      - .actual_access:  write_only
        .address_space:  global
        .offset:         40
        .size:           8
        .value_kind:     global_buffer
      - .actual_access:  read_only
        .address_space:  global
        .offset:         48
        .size:           8
        .value_kind:     global_buffer
    .group_segment_fixed_size: 0
    .kernarg_segment_align: 8
    .kernarg_segment_size: 56
    .language:       OpenCL C
    .language_version:
      - 2
      - 0
    .max_flat_workgroup_size: 768
    .name:           _Z11gemm_kernelILi0ELi6ELi4ELi5EEvPKDF16_S1_PK15HIP_vector_typeIfLj4EEPDF16_S6_S6_Pf
    .private_segment_fixed_size: 0
    .sgpr_count:     56
    .sgpr_spill_count: 0
    .symbol:         _Z11gemm_kernelILi0ELi6ELi4ELi5EEvPKDF16_S1_PK15HIP_vector_typeIfLj4EEPDF16_S6_S6_Pf.kd
    .uniform_work_group_size: 1
    .uses_dynamic_stack: false
    .vgpr_count:     168
    .vgpr_spill_count: 0
    .wavefront_size: 64
  - .agpr_count:     0
    .args:
      - .address_space:  global
        .offset:         0
        .size:           8
        .value_kind:     global_buffer
      - .address_space:  global
        .offset:         8
        .size:           8
        .value_kind:     global_buffer
      - .actual_access:  read_only
        .address_space:  global
        .offset:         16
        .size:           8
        .value_kind:     global_buffer
      - .actual_access:  read_only
        .address_space:  global
        .offset:         24
        .size:           8
        .value_kind:     global_buffer
      - .actual_access:  read_only
        .address_space:  global
        .offset:         32
        .size:           8
        .value_kind:     global_buffer
      - .actual_access:  read_only
        .address_space:  global
        .offset:         40
        .size:           8
        .value_kind:     global_buffer
      - .actual_access:  write_only
        .address_space:  global
        .offset:         48
        .size:           8
        .value_kind:     global_buffer
    .group_segment_fixed_size: 0
    .kernarg_segment_align: 8
    .kernarg_segment_size: 56
    .language:       OpenCL C
    .language_version:
      - 2
      - 0
    .max_flat_workgroup_size: 768
    .name:           _Z11gemm_kernelILi1ELi4ELi2ELi5EEvPKDF16_S1_PK15HIP_vector_typeIfLj4EEPDF16_S6_S6_Pf
    .private_segment_fixed_size: 0
    .sgpr_count:     38
    .sgpr_spill_count: 0
    .symbol:         _Z11gemm_kernelILi1ELi4ELi2ELi5EEvPKDF16_S1_PK15HIP_vector_typeIfLj4EEPDF16_S6_S6_Pf.kd
    .uniform_work_group_size: 1
    .uses_dynamic_stack: false
    .vgpr_count:     66
    .vgpr_spill_count: 0
    .wavefront_size: 64
